# OG intermediate (GLA phase A output) stored tile-major so producer stores and gla_c loads are 512 B contiguous; KVB chunk tensor tile-major (GLA-A stores + scan loads)
# speedup vs baseline: 1.0135x; 1.0056x over previous
.LBB0_809:
	v_readlane_b32 s94, v254, 7
	v_readlane_b32 s95, v254, 8
	s_mov_b64 s[6:7], s[94:95]
	s_cmp_le_i32 s6, s20
	s_cselect_b64 s[4:5], -1, 0
	s_cmp_lt_i32 s20, s7
	s_cselect_b64 s[6:7], -1, 0
	v_mbcnt_lo_u32_b32 v2, -1, 0
	v_mbcnt_hi_u32_b32 v2, -1, v2
	s_and_b64 s[46:47], s[4:5], s[6:7]
	v_or_b32_e32 v0, s66, v2
	s_mov_b32 s92, s71
	v_readfirstlane_b32 s2, v0
	s_andn2_b64 vcc, exec, s[46:47]
	s_cbranch_vccnz .LBB0_934
	s_bitcmp0_b32 s92, 3
	s_cbranch_scc1 .LBB0_837
	s_cmpk_gt_i32 s92, 0x47f
	s_cbranch_scc1 .LBB0_836
	s_add_u32 s78, s44, 0xbcf8000
	s_addc_u32 s79, s45, 0
	s_add_u32 s80, s44, 0x64dc8000
	v_and_b32_e32 v4, 48, v2
	v_mov_b32_e32 v5, v97
	s_addc_u32 s81, s45, 0
	v_lshlrev_b32_e32 v1, 2, v0
	s_ashr_i32 s10, s2, 6
	v_lshl_add_u64 v[6:7], s[44:45], 0, v[4:5]
	s_mov_b64 s[2:3], 0x62548000
	v_ashrrev_i32_e32 v91, 7, v0
	v_readlane_b32 s42, v255, 18
	v_add_u32_e32 v90, 0, v1
	v_lshl_add_u64 v[60:61], v[6:7], 0, s[2:3]
	v_and_b32_e32 v6, 0x1fc, v1
	v_mov_b32_e32 v7, v97
	v_add_u32_e32 v92, s42, v1
	v_lshlrev_b32_e32 v1, 13, v91
	v_lshl_add_u64 v[8:9], s[44:45], 0, v[6:7]
	s_mov_b64 s[2:3], 0x1b118000
	v_add3_u32 v93, 0, v1, v6
	v_ashrrev_i32_e32 v66, 3, v0
	v_lshlrev_b32_e32 v1, 4, v2
	s_movk_i32 s13, 0x110
	v_lshl_add_u64 v[64:65], v[8:9], 0, s[2:3]
	v_and_b32_e32 v8, 0x70, v1
	v_mul_lo_u32 v1, v66, s13
	v_add_u32_e32 v7, 0, v1
	s_movk_i32 s6, 0x80
	v_ashrrev_i32_e32 v1, 31, v0
	v_cmp_gt_i32_e64 s[6:7], s6, v0
	v_lshl_add_u64 v[0:1], v[0:1], 2, s[44:45]
	s_mov_b64 s[14:15], 0x6a7c8000
	v_lshl_add_u64 v[68:69], v[0:1], 0, s[14:15]
	s_lshl_b32 s11, s10, 3
	v_lshlrev_b32_e32 v0, 1, v2
	s_and_b32 s11, s11, 0xfffffe0
	v_and_b32_e32 v0, 24, v0
	v_and_b32_e32 v1, 3, v2
	v_and_b32_e32 v56, 15, v2
	v_or3_b32 v0, v1, v0, s11
	s_lshl_b32 s11, s10, 4
	v_and_b32_e32 v3, 63, v2
	v_bfe_u32 v10, v2, 4, 2
	s_lshl_b32 s8, s10, 5
	v_and_or_b32 v2, s11, 48, v56
	s_and_b32 s11, s10, 0x1ffffffc
	s_lshl_b32 s10, s10, 10
	s_ashr_i32 s9, s8, 31
	s_add_i32 s88, s10, 0
	v_or_b32_e32 v58, s8, v56
	v_mov_b32_e32 v59, s9
	s_add_i32 s88, s88, 0x15000
	s_lshl_b64 s[8:9], s[8:9], 5
	v_mul_lo_u32 v0, v0, s13
	s_add_u32 s8, s44, s8
	v_lshlrev_b32_e32 v96, 3, v10
	v_add_u32_e32 v12, 0, v0
	v_or_b32_e32 v0, s11, v10
	s_addc_u32 s9, s45, s9
	v_lshlrev_b32_e32 v10, 3, v0
	v_lshl_add_u64 v[0:1], s[8:9], 0, v[96:97]
	s_mov_b64 s[8:9], 0x1d518000
	v_lshl_add_u64 v[70:71], v[0:1], 0, s[8:9]
	v_lshl_add_u64 v[0:1], s[44:45], 0, v[96:97]
	v_or_b32_e32 v14, 1, v10
	s_mov_b64 s[82:83], 0x65fc8200
	v_cmp_ge_i32_e64 s[14:15], v14, v2
	v_or_b32_e32 v14, 2, v10
	v_lshl_add_u64 v[74:75], v[0:1], 0, s[82:83]
	s_mov_b64 s[82:83], 0x65fc8400
	v_cmp_le_i32_e64 s[16:17], v14, v2
	v_cmp_ge_i32_e64 s[18:19], v14, v2
	v_or_b32_e32 v14, 3, v10
	v_lshl_add_u64 v[76:77], v[0:1], 0, s[82:83]
	s_mov_b64 s[82:83], 0x65fc8600
	v_cmp_le_i32_e64 s[20:21], v14, v2
	v_cmp_ge_i32_e64 s[22:23], v14, v2
	v_or_b32_e32 v14, 4, v10
	v_lshl_add_u64 v[78:79], v[0:1], 0, s[82:83]
	s_mov_b64 s[82:83], 0x65fc8800
	v_readlane_b32 s12, v255, 19
	s_mov_b64 s[8:9], 0x65fc8000
	v_cmp_le_i32_e64 s[24:25], v14, v2
	v_cmp_ge_i32_e64 s[26:27], v14, v2
	v_or_b32_e32 v14, 5, v10
	v_lshl_add_u64 v[80:81], v[0:1], 0, s[82:83]
	s_mov_b64 s[82:83], 0x65fc8a00
	v_lshl_add_u32 v5, v66, 1, s12
	v_mad_u32_u24 v11, v2, s13, 0
	v_lshlrev_b32_e32 v94, 4, v3
	v_add_u32_e32 v3, s12, v4
	v_lshl_add_u64 v[72:73], v[0:1], 0, s[8:9]
	v_cmp_le_i32_e64 s[8:9], v10, v2
	v_cmp_ge_i32_e64 s[10:11], v10, v2
	v_cmp_lt_i32_e64 s[12:13], v10, v2
	v_cmp_le_i32_e64 s[28:29], v14, v2
	v_cmp_ge_i32_e64 s[30:31], v14, v2
	v_or_b32_e32 v14, 6, v10
	v_or_b32_e32 v10, 7, v10
	v_lshl_add_u64 v[82:83], v[0:1], 0, s[82:83]
	s_mov_b64 s[82:83], 0x65fc8c00
	v_lshlrev_b32_e32 v62, 4, v91
	v_lshlrev_b32_e32 v9, 1, v8
	v_lshl_add_u32 v95, v8, 2, 0
	v_mul_u32_u24_e32 v13, 0x90, v8
	v_cmp_le_i32_e64 s[34:35], v14, v2
	v_cmp_ge_i32_e64 s[36:37], v14, v2
	v_cmp_le_i32_e64 s[38:39], v10, v2
	v_cmp_ge_i32_e64 s[40:41], v10, v2
	v_mul_u32_u24_e32 v2, 0x90, v56
	v_lshl_add_u64 v[84:85], v[0:1], 0, s[82:83]
	s_mov_b64 s[82:83], 0x65fc8e00
	v_readlane_b32 s43, v255, 20
	v_mov_b32_e32 v57, v97
	v_ashrrev_i32_e32 v63, 31, v62
	v_cmp_gt_i32_e64 s[2:3], 3, v91
	v_cmp_lt_i32_e64 s[4:5], 0, v91
	v_ashrrev_i32_e32 v67, 31, v66
	v_lshl_add_u32 v98, v66, 9, v95
	v_lshl_add_u64 v[86:87], v[0:1], 0, s[82:83]
	v_and_b32_e32 v88, 0xffffffe0, v58
	v_lshlrev_b32_e32 v88, 8, v88
	v_and_b32_e32 v89, 15, v58
	v_lshl_or_b32 v88, v89, 5, v88
	v_mov_b32_e32 v89, v97
	v_add_u32_e32 v99, s43, v6
	v_add_u32_e32 v100, s42, v6
	v_lshlrev_b32_e32 v96, 1, v8
	v_add_u32_e32 v101, v5, v13
	v_add_u32_e32 v102, v7, v9
	v_add_u32_e32 v103, v11, v4
	v_add_u32_e32 v104, v12, v4
	v_add_u32_e32 v105, v3, v2
	s_branch .LBB0_814
.LBB0_813:
	s_or_b64 exec, exec, s[84:85]
	s_waitcnt lgkmcnt(0)
	s_barrier
	ds_read_b128 v[0:3], v103 offset:32768
	ds_read_b128 v[4:7], v104 offset:50176
	ds_read_b128 v[8:11], v104 offset:51264
	s_waitcnt lgkmcnt(1)
	v_mfma_f32_16x16x32_bf16 v[4:7], v[4:7], v[0:3], 0
	s_lshl_b32 s76, s89, 5
	s_waitcnt lgkmcnt(0)
	v_mfma_f32_16x16x32_bf16 v[0:3], v[8:11], v[0:3], 0
	ds_read_b128 v[8:11], v103 offset:32832
	ds_read_b128 v[12:15], v104 offset:50240
	ds_read_b128 v[16:19], v104 offset:51328
	s_waitcnt lgkmcnt(1)
	v_mfma_f32_16x16x32_bf16 v[4:7], v[12:15], v[8:11], v[4:7]
	s_waitcnt lgkmcnt(0)
	v_mfma_f32_16x16x32_bf16 v[0:3], v[16:19], v[8:11], v[0:3]
	ds_read_b128 v[8:11], v103 offset:32896
	ds_read_b128 v[12:15], v104 offset:50304
	ds_read_b128 v[16:19], v104 offset:51392
	s_waitcnt lgkmcnt(1)
	v_mfma_f32_16x16x32_bf16 v[4:7], v[12:15], v[8:11], v[4:7]
	s_waitcnt lgkmcnt(0)
	v_mfma_f32_16x16x32_bf16 v[0:3], v[16:19], v[8:11], v[0:3]
	ds_read_b128 v[8:11], v103 offset:32960
	ds_read_b128 v[12:15], v104 offset:50368
	ds_read_b128 v[16:19], v104 offset:51456
	s_waitcnt lgkmcnt(1)
	v_mfma_f32_16x16x32_bf16 v[4:7], v[12:15], v[8:11], v[4:7]
	v_add_u32_e32 v14, 0, v94
	s_waitcnt lgkmcnt(0)
	v_mfma_f32_16x16x32_bf16 v[0:3], v[16:19], v[8:11], v[0:3]
	v_cndmask_b32_e64 v8, 0, 1, s[8:9]
	v_cndmask_b32_e64 v9, 0, 1, s[10:11]
	v_cndmask_b32_e64 v8, v9, v8, s[42:43]
	v_and_b32_e32 v8, 1, v8
	v_cmp_eq_u32_e32 vcc, 1, v8
	v_cndmask_b32_e64 v8, 0, 1, s[12:13]
	v_cndmask_b32_e64 v9, 0, 1, s[14:15]
	v_cndmask_b32_e64 v8, v9, v8, s[42:43]
	v_and_b32_e32 v8, 1, v8
	v_cndmask_b32_e32 v4, 0, v4, vcc
	v_cmp_eq_u32_e32 vcc, 1, v8
	v_cndmask_b32_e64 v8, 0, 1, s[16:17]
	v_cndmask_b32_e64 v9, 0, 1, s[18:19]
	v_cndmask_b32_e64 v8, v9, v8, s[42:43]
	v_and_b32_e32 v8, 1, v8
	v_cndmask_b32_e32 v5, 0, v5, vcc
	v_cmp_eq_u32_e32 vcc, 1, v8
	v_cndmask_b32_e64 v8, 0, 1, s[20:21]
	v_cndmask_b32_e64 v9, 0, 1, s[22:23]
	v_cndmask_b32_e64 v8, v9, v8, s[42:43]
	v_and_b32_e32 v8, 1, v8
	v_cndmask_b32_e32 v6, 0, v6, vcc
	v_cmp_eq_u32_e32 vcc, 1, v8
	v_cndmask_b32_e64 v8, 0, 1, s[24:25]
	v_cndmask_b32_e64 v9, 0, 1, s[26:27]
	v_cndmask_b32_e64 v8, v9, v8, s[42:43]
	v_and_b32_e32 v8, 1, v8
	v_cndmask_b32_e32 v7, 0, v7, vcc
	v_cmp_eq_u32_e32 vcc, 1, v8
	v_cndmask_b32_e64 v9, 0, 1, s[30:31]
	s_nop 0
	v_cndmask_b32_e32 v8, 0, v0, vcc
	v_cndmask_b32_e64 v0, 0, 1, s[28:29]
	v_cndmask_b32_e64 v0, v9, v0, s[42:43]
	v_and_b32_e32 v0, 1, v0
	v_cmp_eq_u32_e32 vcc, 1, v0
	v_cndmask_b32_e64 v0, 0, 1, s[34:35]
	s_nop 0
	v_cndmask_b32_e32 v9, 0, v1, vcc
	v_cndmask_b32_e64 v1, 0, 1, s[36:37]
	v_cndmask_b32_e64 v0, v1, v0, s[42:43]
	v_and_b32_e32 v0, 1, v0
	v_cmp_eq_u32_e32 vcc, 1, v0
	v_cndmask_b32_e64 v0, 0, 1, s[38:39]
	v_cndmask_b32_e64 v1, 0, 1, s[40:41]
	v_cndmask_b32_e64 v0, v1, v0, s[42:43]
	v_and_b32_e32 v0, 1, v0
	v_cndmask_b32_e32 v10, 0, v2, vcc
	v_cmp_eq_u32_e32 vcc, 1, v0
	v_cvt_pk_bf16_f32 v0, v4, v5
	v_cvt_pk_bf16_f32 v1, v6, v7
	v_cndmask_b32_e32 v3, 0, v3, vcc
	v_cvt_pk_bf16_f32 v2, v8, v9
	v_cvt_pk_bf16_f32 v3, v10, v3
	v_add_u32_e32 v4, s88, v94
	ds_write_b128 v4, v[0:3]
	v_add_u32_e32 v0, 0x15000, v14
	s_waitcnt lgkmcnt(0)
	s_barrier
	ds_read_b128 v[0:3], v0
	s_lshl_b64 s[82:83], s[82:83], 11
	v_lshlrev_b32_e32 v8, 5, v56
	v_mov_b32_e32 v9, v97
	v_lshl_add_u64 v[8:9], s[82:83], 0, v[8:9]
	v_add_u32_e32 v4, 0x16000, v14
	v_lshl_add_u64 v[10:11], v[70:71], 0, s[76:77]
	ds_read_b128 v[4:7], v4
	v_lshl_add_u64 v[12:13], v[10:11], 0, v[8:9]
	s_waitcnt lgkmcnt(1)
	v_mfma_f32_16x16x32_bf16 v[8:11], v[44:47], v[0:3], 0
	s_lshl_b64 s[42:43], s[92:93], 16
	s_add_i32 s92, s92, s96
	s_cmpk_lt_i32 s92, 0x480
	v_mfma_f32_16x16x32_bf16 v[0:3], v[36:39], v[0:3], 0
	s_waitcnt lgkmcnt(0)
	v_mfma_f32_16x16x32_bf16 v[0:3], v[32:35], v[4:7], v[0:3]
	v_mfma_f32_16x16x32_bf16 v[8:11], v[40:43], v[4:7], v[8:11]
	v_add_u32_e32 v4, 0x16400, v14
	s_nop 5
	v_cvt_pk_bf16_f32 v0, v0, v1
	v_cvt_pk_bf16_f32 v1, v2, v3
	global_store_dwordx2 v[12:13], v[0:1], off offset:512
	v_add_u32_e32 v0, 0x15400, v14
	ds_read_b128 v[0:3], v0
	ds_read_b128 v[4:7], v4
	v_cvt_pk_bf16_f32 v8, v8, v9
	v_cvt_pk_bf16_f32 v9, v10, v11
	global_store_dwordx2 v[12:13], v[8:9], off
	s_waitcnt lgkmcnt(1)
	v_mfma_f32_16x16x32_bf16 v[8:11], v[44:47], v[0:3], 0
	v_mfma_f32_16x16x32_bf16 v[0:3], v[36:39], v[0:3], 0
	s_waitcnt lgkmcnt(0)
	v_mfma_f32_16x16x32_bf16 v[8:11], v[40:43], v[4:7], v[8:11]
	v_mfma_f32_16x16x32_bf16 v[0:3], v[32:35], v[4:7], v[0:3]
	v_add_u32_e32 v4, 0x16800, v14
	s_nop 5
	v_cvt_pk_bf16_f32 v8, v8, v9
	v_cvt_pk_bf16_f32 v9, v10, v11
	v_add_co_u32_e32 v10, vcc, s65, v12
	ds_read_b128 v[4:7], v4
	s_nop 0
	v_addc_co_u32_e32 v11, vcc, 0, v13, vcc
	v_cvt_pk_bf16_f32 v0, v0, v1
	v_cvt_pk_bf16_f32 v1, v2, v3
	global_store_dwordx2 v[10:11], v[0:1], off offset:512
	v_add_u32_e32 v0, 0x15800, v14
	ds_read_b128 v[0:3], v0
	global_store_dwordx2 v[10:11], v[8:9], off
	s_waitcnt lgkmcnt(0)
	v_mfma_f32_16x16x32_bf16 v[8:11], v[44:47], v[0:3], 0
	v_mfma_f32_16x16x32_bf16 v[0:3], v[36:39], v[0:3], 0
	v_mfma_f32_16x16x32_bf16 v[8:11], v[40:43], v[4:7], v[8:11]
	v_mfma_f32_16x16x32_bf16 v[0:3], v[32:35], v[4:7], v[0:3]
	v_add_u32_e32 v4, 0x16c00, v14
	s_nop 5
	v_cvt_pk_bf16_f32 v8, v8, v9
	v_cvt_pk_bf16_f32 v9, v10, v11
	v_add_co_u32_e32 v10, vcc, s49, v12
	ds_read_b128 v[4:7], v4
	s_nop 0
	v_addc_co_u32_e32 v11, vcc, 0, v13, vcc
	v_cvt_pk_bf16_f32 v0, v0, v1
	v_cvt_pk_bf16_f32 v1, v2, v3
	global_store_dwordx2 v[10:11], v[0:1], off offset:512
	v_add_u32_e32 v0, 0x15c00, v14
	ds_read_b128 v[0:3], v0
	global_store_dwordx2 v[10:11], v[8:9], off
	s_waitcnt lgkmcnt(0)
	v_mfma_f32_16x16x32_bf16 v[8:11], v[44:47], v[0:3], 0
	v_mfma_f32_16x16x32_bf16 v[0:3], v[36:39], v[0:3], 0
	v_mfma_f32_16x16x32_bf16 v[8:11], v[40:43], v[4:7], v[8:11]
	v_mfma_f32_16x16x32_bf16 v[0:3], v[32:35], v[4:7], v[0:3]
	s_nop 6
	v_cvt_pk_bf16_f32 v8, v8, v9
	v_cvt_pk_bf16_f32 v9, v10, v11
	v_add_co_u32_e32 v10, vcc, s64, v12
	v_cvt_pk_bf16_f32 v0, v0, v1
	s_nop 0
	v_addc_co_u32_e32 v11, vcc, 0, v13, vcc
	v_cvt_pk_bf16_f32 v1, v2, v3
	global_store_dwordx2 v[10:11], v[8:9], off
	global_store_dwordx2 v[10:11], v[0:1], off offset:512
	ds_read_b128 v[4:7], v105
	ds_read_b128 v[8:11], v105 offset:64
	s_waitcnt lgkmcnt(1)
	v_mfma_f32_16x16x32_bf16 v[0:3], v[4:7], v[44:47], 0
	v_mfma_f32_16x16x32_bf16 v[4:7], v[4:7], v[36:39], 0
	s_waitcnt lgkmcnt(0)
	v_mfma_f32_16x16x32_bf16 v[0:3], v[8:11], v[40:43], v[0:3]
	v_mfma_f32_16x16x32_bf16 v[4:7], v[8:11], v[32:35], v[4:7]
	s_nop 6
	v_cvt_pk_bf16_f32 v12, v0, v1
	v_lshl_add_u64 v[0:1], s[42:43], 0, v[88:89]
	v_cvt_pk_bf16_f32 v13, v2, v3
	v_lshl_add_u64 v[2:3], v[72:73], 0, v[0:1]
	v_or_b32_e32 v0, 0x1000, v0
	v_cvt_pk_bf16_f32 v4, v4, v5
	v_cvt_pk_bf16_f32 v5, v6, v7
	v_lshl_add_u64 v[6:7], v[72:73], 0, v[0:1]
	global_store_dwordx2 v[2:3], v[12:13], off
	global_store_dwordx2 v[6:7], v[4:5], off
	ds_read_b128 v[4:7], v105 offset:2304
	ds_read_b128 v[8:11], v105 offset:2368
	s_waitcnt lgkmcnt(1)
	v_mfma_f32_16x16x32_bf16 v[12:15], v[4:7], v[44:47], 0
	v_mfma_f32_16x16x32_bf16 v[4:7], v[4:7], v[36:39], 0
	s_waitcnt lgkmcnt(0)
	v_mfma_f32_16x16x32_bf16 v[12:15], v[8:11], v[40:43], v[12:15]
	v_mfma_f32_16x16x32_bf16 v[4:7], v[8:11], v[32:35], v[4:7]
	s_nop 6
	v_cvt_pk_bf16_f32 v12, v12, v13
	v_cvt_pk_bf16_f32 v13, v14, v15
	v_cvt_pk_bf16_f32 v4, v4, v5
	v_cvt_pk_bf16_f32 v5, v6, v7
	v_lshl_add_u64 v[6:7], v[74:75], 0, v[0:1]
	global_store_dwordx2 v[2:3], v[12:13], off offset:512
	global_store_dwordx2 v[6:7], v[4:5], off
	ds_read_b128 v[4:7], v105 offset:4608
	ds_read_b128 v[8:11], v105 offset:4672
	s_waitcnt lgkmcnt(1)
	v_mfma_f32_16x16x32_bf16 v[12:15], v[4:7], v[44:47], 0
	v_mfma_f32_16x16x32_bf16 v[4:7], v[4:7], v[36:39], 0
	s_waitcnt lgkmcnt(0)
	v_mfma_f32_16x16x32_bf16 v[12:15], v[8:11], v[40:43], v[12:15]
	v_mfma_f32_16x16x32_bf16 v[4:7], v[8:11], v[32:35], v[4:7]
	s_nop 6
	v_cvt_pk_bf16_f32 v12, v12, v13
	v_cvt_pk_bf16_f32 v13, v14, v15
	v_cvt_pk_bf16_f32 v4, v4, v5
	v_cvt_pk_bf16_f32 v5, v6, v7
	v_lshl_add_u64 v[6:7], v[76:77], 0, v[0:1]
	global_store_dwordx2 v[2:3], v[12:13], off offset:1024
	global_store_dwordx2 v[6:7], v[4:5], off
	ds_read_b128 v[4:7], v105 offset:6912
	ds_read_b128 v[8:11], v105 offset:6976
	s_waitcnt lgkmcnt(1)
	v_mfma_f32_16x16x32_bf16 v[12:15], v[4:7], v[44:47], 0
	v_mfma_f32_16x16x32_bf16 v[4:7], v[4:7], v[36:39], 0
	s_waitcnt lgkmcnt(0)
	v_mfma_f32_16x16x32_bf16 v[12:15], v[8:11], v[40:43], v[12:15]
	v_mfma_f32_16x16x32_bf16 v[4:7], v[8:11], v[32:35], v[4:7]
	s_nop 6
	v_cvt_pk_bf16_f32 v12, v12, v13
	v_cvt_pk_bf16_f32 v13, v14, v15
	v_cvt_pk_bf16_f32 v4, v4, v5
	v_cvt_pk_bf16_f32 v5, v6, v7
	v_lshl_add_u64 v[6:7], v[78:79], 0, v[0:1]
	global_store_dwordx2 v[2:3], v[12:13], off offset:1536
	global_store_dwordx2 v[6:7], v[4:5], off
	ds_read_b128 v[4:7], v105 offset:9216
	ds_read_b128 v[8:11], v105 offset:9280
	s_waitcnt lgkmcnt(1)
	v_mfma_f32_16x16x32_bf16 v[12:15], v[4:7], v[44:47], 0
	v_mfma_f32_16x16x32_bf16 v[4:7], v[4:7], v[36:39], 0
	s_waitcnt lgkmcnt(0)
	v_mfma_f32_16x16x32_bf16 v[12:15], v[8:11], v[40:43], v[12:15]
	v_mfma_f32_16x16x32_bf16 v[4:7], v[8:11], v[32:35], v[4:7]
	s_nop 6
	v_cvt_pk_bf16_f32 v12, v12, v13
	v_cvt_pk_bf16_f32 v13, v14, v15
	v_cvt_pk_bf16_f32 v4, v4, v5
	v_cvt_pk_bf16_f32 v5, v6, v7
	v_lshl_add_u64 v[6:7], v[80:81], 0, v[0:1]
	global_store_dwordx2 v[2:3], v[12:13], off offset:2048
	global_store_dwordx2 v[6:7], v[4:5], off
	ds_read_b128 v[4:7], v105 offset:11520
	ds_read_b128 v[8:11], v105 offset:11584
	s_waitcnt lgkmcnt(1)
	v_mfma_f32_16x16x32_bf16 v[12:15], v[4:7], v[44:47], 0
	v_mfma_f32_16x16x32_bf16 v[4:7], v[4:7], v[36:39], 0
	s_waitcnt lgkmcnt(0)
	v_mfma_f32_16x16x32_bf16 v[12:15], v[8:11], v[40:43], v[12:15]
	v_mfma_f32_16x16x32_bf16 v[4:7], v[8:11], v[32:35], v[4:7]
	s_nop 6
	v_cvt_pk_bf16_f32 v12, v12, v13
	v_cvt_pk_bf16_f32 v13, v14, v15
	v_cvt_pk_bf16_f32 v4, v4, v5
	v_cvt_pk_bf16_f32 v5, v6, v7
	v_lshl_add_u64 v[6:7], v[82:83], 0, v[0:1]
	global_store_dwordx2 v[2:3], v[12:13], off offset:2560
	global_store_dwordx2 v[6:7], v[4:5], off
	ds_read_b128 v[4:7], v105 offset:13824
	ds_read_b128 v[8:11], v105 offset:13888
	s_waitcnt lgkmcnt(1)
	v_mfma_f32_16x16x32_bf16 v[12:15], v[4:7], v[44:47], 0
	v_mfma_f32_16x16x32_bf16 v[4:7], v[4:7], v[36:39], 0
	s_waitcnt lgkmcnt(0)
	v_mfma_f32_16x16x32_bf16 v[12:15], v[8:11], v[40:43], v[12:15]
	v_mfma_f32_16x16x32_bf16 v[4:7], v[8:11], v[32:35], v[4:7]
	s_nop 6
	v_cvt_pk_bf16_f32 v12, v12, v13
	v_cvt_pk_bf16_f32 v13, v14, v15
	v_cvt_pk_bf16_f32 v4, v4, v5
	v_cvt_pk_bf16_f32 v5, v6, v7
	v_lshl_add_u64 v[6:7], v[84:85], 0, v[0:1]
	global_store_dwordx2 v[2:3], v[12:13], off offset:3072
	global_store_dwordx2 v[6:7], v[4:5], off
	ds_read_b128 v[4:7], v105 offset:16128
	ds_read_b128 v[8:11], v105 offset:16192
	s_waitcnt lgkmcnt(1)
	v_mfma_f32_16x16x32_bf16 v[12:15], v[4:7], v[44:47], 0
	v_lshl_add_u64 v[0:1], v[86:87], 0, v[0:1]
	s_waitcnt lgkmcnt(0)
	v_mfma_f32_16x16x32_bf16 v[12:15], v[8:11], v[40:43], v[12:15]
	s_nop 7
	v_cvt_pk_bf16_f32 v12, v12, v13
	v_cvt_pk_bf16_f32 v13, v14, v15
	global_store_dwordx2 v[2:3], v[12:13], off offset:3584
	v_mfma_f32_16x16x32_bf16 v[2:5], v[4:7], v[36:39], 0
	v_mfma_f32_16x16x32_bf16 v[2:5], v[8:11], v[32:35], v[2:5]
	s_nop 7
	v_cvt_pk_bf16_f32 v2, v2, v3
	v_cvt_pk_bf16_f32 v3, v4, v5
	global_store_dwordx2 v[0:1], v[2:3], off
	s_cbranch_scc0 .LBB0_836

.LBB0_907:
	v_mbcnt_lo_u32_b32 v2, -1, 0
	v_mbcnt_hi_u32_b32 v2, -1, v2
	s_mov_b32 s78, s71
	v_or_b32_e32 v0, s66, v2
	s_bitcmp1_b32 s78, 3
	v_readfirstlane_b32 s2, v0
	s_cbranch_scc1 .LBB0_934
	s_cmpk_gt_i32 s78, 0x47f
	s_cbranch_scc1 .LBB0_933
	s_add_u32 s80, s44, 0xbcf8000
	s_addc_u32 s81, s45, 0
	s_add_u32 s82, s44, 0x64dc8000
	v_and_b32_e32 v4, 48, v2
	v_mov_b32_e32 v5, v97
	s_addc_u32 s83, s45, 0
	v_lshlrev_b32_e32 v1, 2, v0
	s_ashr_i32 s10, s2, 6
	v_lshl_add_u64 v[6:7], s[44:45], 0, v[4:5]
	s_mov_b64 s[2:3], 0x62548000
	v_ashrrev_i32_e32 v91, 7, v0
	v_readlane_b32 s42, v255, 18
	v_add_u32_e32 v90, 0, v1
	v_lshl_add_u64 v[60:61], v[6:7], 0, s[2:3]
	v_and_b32_e32 v6, 0x1fc, v1
	v_mov_b32_e32 v7, v97
	v_add_u32_e32 v92, s42, v1
	v_lshlrev_b32_e32 v1, 13, v91
	v_lshl_add_u64 v[8:9], s[44:45], 0, v[6:7]
	s_mov_b64 s[2:3], 0x1b118000
	v_add3_u32 v93, 0, v1, v6
	v_ashrrev_i32_e32 v66, 3, v0
	v_lshlrev_b32_e32 v1, 4, v2
	s_movk_i32 s13, 0x110
	v_lshl_add_u64 v[64:65], v[8:9], 0, s[2:3]
	v_and_b32_e32 v8, 0x70, v1
	v_mul_lo_u32 v1, v66, s13
	v_add_u32_e32 v7, 0, v1
	s_movk_i32 s6, 0x80
	v_ashrrev_i32_e32 v1, 31, v0
	v_cmp_gt_i32_e64 s[6:7], s6, v0
	v_lshl_add_u64 v[0:1], v[0:1], 2, s[44:45]
	s_mov_b64 s[14:15], 0x6a7c8000
	v_lshl_add_u64 v[68:69], v[0:1], 0, s[14:15]
	s_lshl_b32 s11, s10, 3
	v_lshlrev_b32_e32 v0, 1, v2
	s_and_b32 s11, s11, 0xfffffe0
	v_and_b32_e32 v0, 24, v0
	v_and_b32_e32 v1, 3, v2
	v_and_b32_e32 v56, 15, v2
	v_or3_b32 v0, v1, v0, s11
	s_lshl_b32 s11, s10, 4
	v_and_b32_e32 v3, 63, v2
	v_bfe_u32 v10, v2, 4, 2
	s_lshl_b32 s8, s10, 5
	v_and_or_b32 v2, s11, 48, v56
	s_and_b32 s11, s10, 0x1ffffffc
	s_lshl_b32 s10, s10, 10
	s_ashr_i32 s9, s8, 31
	s_add_i32 s90, s10, 0
	v_or_b32_e32 v58, s8, v56
	v_mov_b32_e32 v59, s9
	s_add_i32 s90, s90, 0x15000
	s_lshl_b64 s[8:9], s[8:9], 5
	v_mul_lo_u32 v0, v0, s13
	s_add_u32 s8, s44, s8
	v_lshlrev_b32_e32 v96, 3, v10
	v_add_u32_e32 v12, 0, v0
	v_or_b32_e32 v0, s11, v10
	s_addc_u32 s9, s45, s9
	v_lshlrev_b32_e32 v10, 3, v0
	v_lshl_add_u64 v[0:1], s[8:9], 0, v[96:97]
	s_mov_b64 s[8:9], 0x1d518000
	v_lshl_add_u64 v[70:71], v[0:1], 0, s[8:9]
	v_lshl_add_u64 v[0:1], s[44:45], 0, v[96:97]
	v_or_b32_e32 v14, 1, v10
	s_mov_b64 s[84:85], 0x65fc8200
	v_cmp_ge_i32_e64 s[14:15], v14, v2
	v_or_b32_e32 v14, 2, v10
	v_lshl_add_u64 v[74:75], v[0:1], 0, s[84:85]
	s_mov_b64 s[84:85], 0x65fc8400
	v_cmp_le_i32_e64 s[16:17], v14, v2
	v_cmp_ge_i32_e64 s[18:19], v14, v2
	v_or_b32_e32 v14, 3, v10
	v_lshl_add_u64 v[76:77], v[0:1], 0, s[84:85]
	s_mov_b64 s[84:85], 0x65fc8600
	v_cmp_le_i32_e64 s[20:21], v14, v2
	v_cmp_ge_i32_e64 s[22:23], v14, v2
	v_or_b32_e32 v14, 4, v10
	v_lshl_add_u64 v[78:79], v[0:1], 0, s[84:85]
	s_mov_b64 s[84:85], 0x65fc8800
	v_readlane_b32 s12, v255, 19
	s_mov_b64 s[8:9], 0x65fc8000
	v_cmp_le_i32_e64 s[24:25], v14, v2
	v_cmp_ge_i32_e64 s[26:27], v14, v2
	v_or_b32_e32 v14, 5, v10
	v_lshl_add_u64 v[80:81], v[0:1], 0, s[84:85]
	s_mov_b64 s[84:85], 0x65fc8a00
	v_lshl_add_u32 v5, v66, 1, s12
	v_mad_u32_u24 v11, v2, s13, 0
	v_lshlrev_b32_e32 v94, 4, v3
	v_add_u32_e32 v3, s12, v4
	v_lshl_add_u64 v[72:73], v[0:1], 0, s[8:9]
	v_cmp_le_i32_e64 s[8:9], v10, v2
	v_cmp_ge_i32_e64 s[10:11], v10, v2
	v_cmp_lt_i32_e64 s[12:13], v10, v2
	v_cmp_le_i32_e64 s[28:29], v14, v2
	v_cmp_ge_i32_e64 s[30:31], v14, v2
	v_or_b32_e32 v14, 6, v10
	v_or_b32_e32 v10, 7, v10
	v_lshl_add_u64 v[82:83], v[0:1], 0, s[84:85]
	s_mov_b64 s[84:85], 0x65fc8c00
	v_lshlrev_b32_e32 v62, 4, v91
	v_lshlrev_b32_e32 v9, 1, v8
	v_lshl_add_u32 v95, v8, 2, 0
	v_mul_u32_u24_e32 v13, 0x90, v8
	v_cmp_le_i32_e64 s[34:35], v14, v2
	v_cmp_ge_i32_e64 s[36:37], v14, v2
	v_cmp_le_i32_e64 s[38:39], v10, v2
	v_cmp_ge_i32_e64 s[40:41], v10, v2
	v_mul_u32_u24_e32 v2, 0x90, v56
	v_lshl_add_u64 v[84:85], v[0:1], 0, s[84:85]
	s_mov_b64 s[84:85], 0x65fc8e00
	v_readlane_b32 s43, v255, 20
	v_mov_b32_e32 v57, v97
	v_ashrrev_i32_e32 v63, 31, v62
	v_cmp_gt_i32_e64 s[2:3], 3, v91
	v_cmp_lt_i32_e64 s[4:5], 0, v91
	v_ashrrev_i32_e32 v67, 31, v66
	v_lshl_add_u32 v98, v66, 9, v95
	v_lshl_add_u64 v[86:87], v[0:1], 0, s[84:85]
	v_and_b32_e32 v88, 0xffffffe0, v58
	v_lshlrev_b32_e32 v88, 8, v88
	v_and_b32_e32 v89, 15, v58
	v_lshl_or_b32 v88, v89, 5, v88
	v_mov_b32_e32 v89, v97
	v_add_u32_e32 v99, s43, v6
	v_add_u32_e32 v100, s42, v6
	v_lshlrev_b32_e32 v96, 1, v8
	v_add_u32_e32 v101, v5, v13
	v_add_u32_e32 v102, v7, v9
	v_add_u32_e32 v103, v11, v4
	v_add_u32_e32 v104, v12, v4
	v_add_u32_e32 v105, v3, v2
	s_branch .LBB0_911
.LBB0_910:
	s_or_b64 exec, exec, s[86:87]
	s_waitcnt lgkmcnt(0)
	s_barrier
	ds_read_b128 v[0:3], v103 offset:32768
	ds_read_b128 v[4:7], v104 offset:50176
	ds_read_b128 v[8:11], v104 offset:51264
	s_waitcnt lgkmcnt(1)
	v_mfma_f32_16x16x32_bf16 v[4:7], v[4:7], v[0:3], 0
	s_lshl_b32 s76, s91, 5
	s_waitcnt lgkmcnt(0)
	v_mfma_f32_16x16x32_bf16 v[0:3], v[8:11], v[0:3], 0
	ds_read_b128 v[8:11], v103 offset:32832
	ds_read_b128 v[12:15], v104 offset:50240
	ds_read_b128 v[16:19], v104 offset:51328
	s_waitcnt lgkmcnt(1)
	v_mfma_f32_16x16x32_bf16 v[4:7], v[12:15], v[8:11], v[4:7]
	s_waitcnt lgkmcnt(0)
	v_mfma_f32_16x16x32_bf16 v[0:3], v[16:19], v[8:11], v[0:3]
	ds_read_b128 v[8:11], v103 offset:32896
	ds_read_b128 v[12:15], v104 offset:50304
	ds_read_b128 v[16:19], v104 offset:51392
	s_waitcnt lgkmcnt(1)
	v_mfma_f32_16x16x32_bf16 v[4:7], v[12:15], v[8:11], v[4:7]
	s_waitcnt lgkmcnt(0)
	v_mfma_f32_16x16x32_bf16 v[0:3], v[16:19], v[8:11], v[0:3]
	ds_read_b128 v[8:11], v103 offset:32960
	ds_read_b128 v[12:15], v104 offset:50368
	ds_read_b128 v[16:19], v104 offset:51456
	s_waitcnt lgkmcnt(1)
	v_mfma_f32_16x16x32_bf16 v[4:7], v[12:15], v[8:11], v[4:7]
	v_add_u32_e32 v14, 0, v94
	s_waitcnt lgkmcnt(0)
	v_mfma_f32_16x16x32_bf16 v[0:3], v[16:19], v[8:11], v[0:3]
	v_cndmask_b32_e64 v8, 0, 1, s[8:9]
	v_cndmask_b32_e64 v9, 0, 1, s[10:11]
	v_cndmask_b32_e64 v8, v9, v8, s[42:43]
	v_and_b32_e32 v8, 1, v8
	v_cmp_eq_u32_e32 vcc, 1, v8
	v_cndmask_b32_e64 v8, 0, 1, s[12:13]
	v_cndmask_b32_e64 v9, 0, 1, s[14:15]
	v_cndmask_b32_e64 v8, v9, v8, s[42:43]
	v_and_b32_e32 v8, 1, v8
	v_cndmask_b32_e32 v4, 0, v4, vcc
	v_cmp_eq_u32_e32 vcc, 1, v8
	v_cndmask_b32_e64 v8, 0, 1, s[16:17]
	v_cndmask_b32_e64 v9, 0, 1, s[18:19]
	v_cndmask_b32_e64 v8, v9, v8, s[42:43]
	v_and_b32_e32 v8, 1, v8
	v_cndmask_b32_e32 v5, 0, v5, vcc
	v_cmp_eq_u32_e32 vcc, 1, v8
	v_cndmask_b32_e64 v8, 0, 1, s[20:21]
	v_cndmask_b32_e64 v9, 0, 1, s[22:23]
	v_cndmask_b32_e64 v8, v9, v8, s[42:43]
	v_and_b32_e32 v8, 1, v8
	v_cndmask_b32_e32 v6, 0, v6, vcc
	v_cmp_eq_u32_e32 vcc, 1, v8
	v_cndmask_b32_e64 v8, 0, 1, s[24:25]
	v_cndmask_b32_e64 v9, 0, 1, s[26:27]
	v_cndmask_b32_e64 v8, v9, v8, s[42:43]
	v_and_b32_e32 v8, 1, v8
	v_cndmask_b32_e32 v7, 0, v7, vcc
	v_cmp_eq_u32_e32 vcc, 1, v8
	v_cndmask_b32_e64 v9, 0, 1, s[30:31]
	s_nop 0
	v_cndmask_b32_e32 v8, 0, v0, vcc
	v_cndmask_b32_e64 v0, 0, 1, s[28:29]
	v_cndmask_b32_e64 v0, v9, v0, s[42:43]
	v_and_b32_e32 v0, 1, v0
	v_cmp_eq_u32_e32 vcc, 1, v0
	v_cndmask_b32_e64 v0, 0, 1, s[34:35]
	s_nop 0
	v_cndmask_b32_e32 v9, 0, v1, vcc
	v_cndmask_b32_e64 v1, 0, 1, s[36:37]
	v_cndmask_b32_e64 v0, v1, v0, s[42:43]
	v_and_b32_e32 v0, 1, v0
	v_cmp_eq_u32_e32 vcc, 1, v0
	v_cndmask_b32_e64 v0, 0, 1, s[38:39]
	v_cndmask_b32_e64 v1, 0, 1, s[40:41]
	v_cndmask_b32_e64 v0, v1, v0, s[42:43]
	v_and_b32_e32 v0, 1, v0
	v_cndmask_b32_e32 v10, 0, v2, vcc
	v_cmp_eq_u32_e32 vcc, 1, v0
	v_cvt_pk_bf16_f32 v0, v4, v5
	v_cvt_pk_bf16_f32 v1, v6, v7
	v_cndmask_b32_e32 v3, 0, v3, vcc
	v_cvt_pk_bf16_f32 v2, v8, v9
	v_cvt_pk_bf16_f32 v3, v10, v3
	v_add_u32_e32 v4, s90, v94
	ds_write_b128 v4, v[0:3]
	v_add_u32_e32 v0, 0x15000, v14
	s_waitcnt lgkmcnt(0)
	s_barrier
	ds_read_b128 v[0:3], v0
	s_lshl_b64 s[84:85], s[84:85], 11
	v_lshlrev_b32_e32 v8, 5, v56
	v_mov_b32_e32 v9, v97
	v_lshl_add_u64 v[8:9], s[84:85], 0, v[8:9]
	v_add_u32_e32 v4, 0x16000, v14
	v_lshl_add_u64 v[10:11], v[70:71], 0, s[76:77]
	ds_read_b128 v[4:7], v4
	v_lshl_add_u64 v[12:13], v[10:11], 0, v[8:9]
	s_waitcnt lgkmcnt(1)
	v_mfma_f32_16x16x32_bf16 v[8:11], v[44:47], v[0:3], 0
	s_lshl_b64 s[42:43], s[78:79], 16
	s_add_i32 s78, s78, s96
	s_cmpk_lt_i32 s78, 0x480
	v_mfma_f32_16x16x32_bf16 v[0:3], v[36:39], v[0:3], 0
	s_waitcnt lgkmcnt(0)
	v_mfma_f32_16x16x32_bf16 v[0:3], v[32:35], v[4:7], v[0:3]
	v_mfma_f32_16x16x32_bf16 v[8:11], v[40:43], v[4:7], v[8:11]
	v_add_u32_e32 v4, 0x16400, v14
	s_nop 5
	v_cvt_pk_bf16_f32 v0, v0, v1
	v_cvt_pk_bf16_f32 v1, v2, v3
	global_store_dwordx2 v[12:13], v[0:1], off offset:512
	v_add_u32_e32 v0, 0x15400, v14
	ds_read_b128 v[0:3], v0
	ds_read_b128 v[4:7], v4
	v_cvt_pk_bf16_f32 v8, v8, v9
	v_cvt_pk_bf16_f32 v9, v10, v11
	global_store_dwordx2 v[12:13], v[8:9], off
	s_waitcnt lgkmcnt(1)
	v_mfma_f32_16x16x32_bf16 v[8:11], v[44:47], v[0:3], 0
	v_mfma_f32_16x16x32_bf16 v[0:3], v[36:39], v[0:3], 0
	s_waitcnt lgkmcnt(0)
	v_mfma_f32_16x16x32_bf16 v[8:11], v[40:43], v[4:7], v[8:11]
	v_mfma_f32_16x16x32_bf16 v[0:3], v[32:35], v[4:7], v[0:3]
	v_add_u32_e32 v4, 0x16800, v14
	s_nop 5
	v_cvt_pk_bf16_f32 v8, v8, v9
	v_cvt_pk_bf16_f32 v9, v10, v11
	v_add_co_u32_e32 v10, vcc, s65, v12
	ds_read_b128 v[4:7], v4
	s_nop 0
	v_addc_co_u32_e32 v11, vcc, 0, v13, vcc
	v_cvt_pk_bf16_f32 v0, v0, v1
	v_cvt_pk_bf16_f32 v1, v2, v3
	global_store_dwordx2 v[10:11], v[0:1], off offset:512
	v_add_u32_e32 v0, 0x15800, v14
	ds_read_b128 v[0:3], v0
	global_store_dwordx2 v[10:11], v[8:9], off
	s_waitcnt lgkmcnt(0)
	v_mfma_f32_16x16x32_bf16 v[8:11], v[44:47], v[0:3], 0
	v_mfma_f32_16x16x32_bf16 v[0:3], v[36:39], v[0:3], 0
	v_mfma_f32_16x16x32_bf16 v[8:11], v[40:43], v[4:7], v[8:11]
	v_mfma_f32_16x16x32_bf16 v[0:3], v[32:35], v[4:7], v[0:3]
	v_add_u32_e32 v4, 0x16c00, v14
	s_nop 5
	v_cvt_pk_bf16_f32 v8, v8, v9
	v_cvt_pk_bf16_f32 v9, v10, v11
	v_add_co_u32_e32 v10, vcc, s49, v12
	ds_read_b128 v[4:7], v4
	s_nop 0
	v_addc_co_u32_e32 v11, vcc, 0, v13, vcc
	v_cvt_pk_bf16_f32 v0, v0, v1
	v_cvt_pk_bf16_f32 v1, v2, v3
	global_store_dwordx2 v[10:11], v[0:1], off offset:512
	v_add_u32_e32 v0, 0x15c00, v14
	ds_read_b128 v[0:3], v0
	global_store_dwordx2 v[10:11], v[8:9], off
	s_waitcnt lgkmcnt(0)
	v_mfma_f32_16x16x32_bf16 v[8:11], v[44:47], v[0:3], 0
	v_mfma_f32_16x16x32_bf16 v[0:3], v[36:39], v[0:3], 0
	v_mfma_f32_16x16x32_bf16 v[8:11], v[40:43], v[4:7], v[8:11]
	v_mfma_f32_16x16x32_bf16 v[0:3], v[32:35], v[4:7], v[0:3]
	s_nop 6
	v_cvt_pk_bf16_f32 v8, v8, v9
	v_cvt_pk_bf16_f32 v9, v10, v11
	v_add_co_u32_e32 v10, vcc, s64, v12
	v_cvt_pk_bf16_f32 v0, v0, v1
	s_nop 0
	v_addc_co_u32_e32 v11, vcc, 0, v13, vcc
	v_cvt_pk_bf16_f32 v1, v2, v3
	global_store_dwordx2 v[10:11], v[8:9], off
	global_store_dwordx2 v[10:11], v[0:1], off offset:512
	ds_read_b128 v[4:7], v105
	ds_read_b128 v[8:11], v105 offset:64
	s_waitcnt lgkmcnt(1)
	v_mfma_f32_16x16x32_bf16 v[0:3], v[4:7], v[44:47], 0
	v_mfma_f32_16x16x32_bf16 v[4:7], v[4:7], v[36:39], 0
	s_waitcnt lgkmcnt(0)
	v_mfma_f32_16x16x32_bf16 v[0:3], v[8:11], v[40:43], v[0:3]
	v_mfma_f32_16x16x32_bf16 v[4:7], v[8:11], v[32:35], v[4:7]
	s_nop 6
	v_cvt_pk_bf16_f32 v12, v0, v1
	v_lshl_add_u64 v[0:1], s[42:43], 0, v[88:89]
	v_cvt_pk_bf16_f32 v13, v2, v3
	v_lshl_add_u64 v[2:3], v[72:73], 0, v[0:1]
	v_or_b32_e32 v0, 0x1000, v0
	v_cvt_pk_bf16_f32 v4, v4, v5
	v_cvt_pk_bf16_f32 v5, v6, v7
	v_lshl_add_u64 v[6:7], v[72:73], 0, v[0:1]
	global_store_dwordx2 v[2:3], v[12:13], off
	global_store_dwordx2 v[6:7], v[4:5], off
	ds_read_b128 v[4:7], v105 offset:2304
	ds_read_b128 v[8:11], v105 offset:2368
	s_waitcnt lgkmcnt(1)
	v_mfma_f32_16x16x32_bf16 v[12:15], v[4:7], v[44:47], 0
	v_mfma_f32_16x16x32_bf16 v[4:7], v[4:7], v[36:39], 0
	s_waitcnt lgkmcnt(0)
	v_mfma_f32_16x16x32_bf16 v[12:15], v[8:11], v[40:43], v[12:15]
	v_mfma_f32_16x16x32_bf16 v[4:7], v[8:11], v[32:35], v[4:7]
	s_nop 6
	v_cvt_pk_bf16_f32 v12, v12, v13
	v_cvt_pk_bf16_f32 v13, v14, v15
	v_cvt_pk_bf16_f32 v4, v4, v5
	v_cvt_pk_bf16_f32 v5, v6, v7
	v_lshl_add_u64 v[6:7], v[74:75], 0, v[0:1]
	global_store_dwordx2 v[2:3], v[12:13], off offset:512
	global_store_dwordx2 v[6:7], v[4:5], off
	ds_read_b128 v[4:7], v105 offset:4608
	ds_read_b128 v[8:11], v105 offset:4672
	s_waitcnt lgkmcnt(1)
	v_mfma_f32_16x16x32_bf16 v[12:15], v[4:7], v[44:47], 0
	v_mfma_f32_16x16x32_bf16 v[4:7], v[4:7], v[36:39], 0
	s_waitcnt lgkmcnt(0)
	v_mfma_f32_16x16x32_bf16 v[12:15], v[8:11], v[40:43], v[12:15]
	v_mfma_f32_16x16x32_bf16 v[4:7], v[8:11], v[32:35], v[4:7]
	s_nop 6
	v_cvt_pk_bf16_f32 v12, v12, v13
	v_cvt_pk_bf16_f32 v13, v14, v15
	v_cvt_pk_bf16_f32 v4, v4, v5
	v_cvt_pk_bf16_f32 v5, v6, v7
	v_lshl_add_u64 v[6:7], v[76:77], 0, v[0:1]
	global_store_dwordx2 v[2:3], v[12:13], off offset:1024
	global_store_dwordx2 v[6:7], v[4:5], off
	ds_read_b128 v[4:7], v105 offset:6912
	ds_read_b128 v[8:11], v105 offset:6976
	s_waitcnt lgkmcnt(1)
	v_mfma_f32_16x16x32_bf16 v[12:15], v[4:7], v[44:47], 0
	v_mfma_f32_16x16x32_bf16 v[4:7], v[4:7], v[36:39], 0
	s_waitcnt lgkmcnt(0)
	v_mfma_f32_16x16x32_bf16 v[12:15], v[8:11], v[40:43], v[12:15]
	v_mfma_f32_16x16x32_bf16 v[4:7], v[8:11], v[32:35], v[4:7]
	s_nop 6
	v_cvt_pk_bf16_f32 v12, v12, v13
	v_cvt_pk_bf16_f32 v13, v14, v15
	v_cvt_pk_bf16_f32 v4, v4, v5
	v_cvt_pk_bf16_f32 v5, v6, v7
	v_lshl_add_u64 v[6:7], v[78:79], 0, v[0:1]
	global_store_dwordx2 v[2:3], v[12:13], off offset:1536
	global_store_dwordx2 v[6:7], v[4:5], off
	ds_read_b128 v[4:7], v105 offset:9216
	ds_read_b128 v[8:11], v105 offset:9280
	s_waitcnt lgkmcnt(1)
	v_mfma_f32_16x16x32_bf16 v[12:15], v[4:7], v[44:47], 0
	v_mfma_f32_16x16x32_bf16 v[4:7], v[4:7], v[36:39], 0
	s_waitcnt lgkmcnt(0)
	v_mfma_f32_16x16x32_bf16 v[12:15], v[8:11], v[40:43], v[12:15]
	v_mfma_f32_16x16x32_bf16 v[4:7], v[8:11], v[32:35], v[4:7]
	s_nop 6
	v_cvt_pk_bf16_f32 v12, v12, v13
	v_cvt_pk_bf16_f32 v13, v14, v15
	v_cvt_pk_bf16_f32 v4, v4, v5
	v_cvt_pk_bf16_f32 v5, v6, v7
	v_lshl_add_u64 v[6:7], v[80:81], 0, v[0:1]
	global_store_dwordx2 v[2:3], v[12:13], off offset:2048
	global_store_dwordx2 v[6:7], v[4:5], off
	ds_read_b128 v[4:7], v105 offset:11520
	ds_read_b128 v[8:11], v105 offset:11584
	s_waitcnt lgkmcnt(1)
	v_mfma_f32_16x16x32_bf16 v[12:15], v[4:7], v[44:47], 0
	v_mfma_f32_16x16x32_bf16 v[4:7], v[4:7], v[36:39], 0
	s_waitcnt lgkmcnt(0)
	v_mfma_f32_16x16x32_bf16 v[12:15], v[8:11], v[40:43], v[12:15]
	v_mfma_f32_16x16x32_bf16 v[4:7], v[8:11], v[32:35], v[4:7]
	s_nop 6
	v_cvt_pk_bf16_f32 v12, v12, v13
	v_cvt_pk_bf16_f32 v13, v14, v15
	v_cvt_pk_bf16_f32 v4, v4, v5
	v_cvt_pk_bf16_f32 v5, v6, v7
	v_lshl_add_u64 v[6:7], v[82:83], 0, v[0:1]
	global_store_dwordx2 v[2:3], v[12:13], off offset:2560
	global_store_dwordx2 v[6:7], v[4:5], off
	ds_read_b128 v[4:7], v105 offset:13824
	ds_read_b128 v[8:11], v105 offset:13888
	s_waitcnt lgkmcnt(1)
	v_mfma_f32_16x16x32_bf16 v[12:15], v[4:7], v[44:47], 0
	v_mfma_f32_16x16x32_bf16 v[4:7], v[4:7], v[36:39], 0
	s_waitcnt lgkmcnt(0)
	v_mfma_f32_16x16x32_bf16 v[12:15], v[8:11], v[40:43], v[12:15]
	v_mfma_f32_16x16x32_bf16 v[4:7], v[8:11], v[32:35], v[4:7]
	s_nop 6
	v_cvt_pk_bf16_f32 v12, v12, v13
	v_cvt_pk_bf16_f32 v13, v14, v15
	v_cvt_pk_bf16_f32 v4, v4, v5
	v_cvt_pk_bf16_f32 v5, v6, v7
	v_lshl_add_u64 v[6:7], v[84:85], 0, v[0:1]
	global_store_dwordx2 v[2:3], v[12:13], off offset:3072
	global_store_dwordx2 v[6:7], v[4:5], off
	ds_read_b128 v[4:7], v105 offset:16128
	ds_read_b128 v[8:11], v105 offset:16192
	s_waitcnt lgkmcnt(1)
	v_mfma_f32_16x16x32_bf16 v[12:15], v[4:7], v[44:47], 0
	v_lshl_add_u64 v[0:1], v[86:87], 0, v[0:1]
	s_waitcnt lgkmcnt(0)
	v_mfma_f32_16x16x32_bf16 v[12:15], v[8:11], v[40:43], v[12:15]
	s_nop 7
	v_cvt_pk_bf16_f32 v12, v12, v13
	v_cvt_pk_bf16_f32 v13, v14, v15
	global_store_dwordx2 v[2:3], v[12:13], off offset:3584
	v_mfma_f32_16x16x32_bf16 v[2:5], v[4:7], v[36:39], 0
	v_mfma_f32_16x16x32_bf16 v[2:5], v[8:11], v[32:35], v[2:5]
	s_nop 7
	v_cvt_pk_bf16_f32 v2, v2, v3
	v_cvt_pk_bf16_f32 v3, v4, v5
	global_store_dwordx2 v[0:1], v[2:3], off
	s_cbranch_scc0 .LBB0_933

.LBB0_1058:
	s_and_b32 s9, s12, 3
	v_add_u32_e32 v52, s11, v62
	v_ashrrev_i32_e32 v53, 31, v52
	s_lshl_b32 s8, s9, 8
	v_lshlrev_b64 v[54:55], 11, v[52:53]
	v_and_b32_e32 v2, 0xfffffff0, v52
	v_mov_b32_e32 v3, v53
	v_lshlrev_b64 v[2:3], 11, v[2:3]
	v_lshl_add_u64 v[2:3], s[4:5], 0, v[2:3]
	v_and_b32_e32 v0, 15, v52
	v_lshlrev_b32_e32 v0, 5, v0
	v_lshl_add_u32 v0, s9, 13, v0
	v_and_b32_e32 v1, 0x80, v44
	v_lshl_add_u32 v0, v1, 5, v0
	v_and_b32_e32 v1, 12, v44
	v_lshl_add_u32 v0, v1, 1, v0
	v_mov_b32_e32 v1, v97
	v_lshl_add_u64 v[0:1], v[2:3], 0, v[0:1]
	s_mov_b64 s[18:19], 0x1200000
	v_add_co_u32_e32 v28, vcc, 0x1200000, v0
	v_lshl_add_u64 v[16:17], v[0:1], 0, s[18:19]
	s_nop 0
	v_addc_co_u32_e32 v29, vcc, 0, v1, vcc
	global_load_dwordx2 v[2:3], v[0:1], off
	global_load_dwordx2 v[4:5], v[0:1], off offset:512
	global_load_dwordx2 v[6:7], v[0:1], off offset:1024
	global_load_dwordx2 v[8:9], v[0:1], off offset:1536
	global_load_dwordx2 v[10:11], v[0:1], off offset:2048
	global_load_dwordx2 v[12:13], v[0:1], off offset:2560
	global_load_dwordx2 v[14:15], v[0:1], off offset:3072
	global_load_dwordx2 v[18:19], v[16:17], off offset:512
	global_load_dwordx2 v[20:21], v[16:17], off offset:1024
	global_load_dwordx2 v[22:23], v[16:17], off offset:1536
	global_load_dwordx2 v[24:25], v[16:17], off offset:2048
	global_load_dwordx2 v[26:27], v[16:17], off offset:2560
	global_load_dwordx2 v[30:31], v[16:17], off offset:3072
	s_nop 0
	global_load_dwordx2 v[28:29], v[28:29], off
	s_nop 0
	global_load_dwordx2 v[0:1], v[0:1], off offset:3584
	s_nop 0
	global_load_dwordx2 v[16:17], v[16:17], off offset:3584
	s_lshl_b32 s10, s10, 2
	s_or_b32 s18, s10, s9
	s_mov_b32 s9, s77
	s_ashr_i32 s19, s17, 31
	v_lshl_add_u64 v[94:95], v[46:47], 0, s[8:9]
	v_mov_b64_e32 v[86:87], s[44:45]
	v_mad_i64_i32 v[86:87], s[20:21], v52, s59, v[86:87]
	s_lshl_b32 s76, s8, 1
	v_lshl_add_u64 v[86:87], v[86:87], 0, s[76:77]
	v_lshlrev_b64 v[92:93], 1, v[44:45]
	v_lshl_add_u64 v[86:87], v[86:87], 0, v[92:93]
	s_mov_b64 s[20:21], 0xbcfa800
	v_lshl_add_u64 v[86:87], v[86:87], 0, s[20:21]
	global_load_dwordx2 v[184:185], v[86:87], off
	global_load_dwordx4 v[200:203], v[48:49], off
	global_load_dwordx2 v[186:187], v[86:87], off offset:32
	global_load_dwordx4 v[204:207], v[48:49], off offset:64
	global_load_dwordx2 v[188:189], v[86:87], off offset:64
	global_load_dwordx4 v[208:211], v[48:49], off offset:128
	global_load_dwordx2 v[190:191], v[86:87], off offset:96
	global_load_dwordx4 v[212:215], v[48:49], off offset:192
	global_load_dwordx2 v[192:193], v[86:87], off offset:128
	global_load_dwordx4 v[218:221], v[48:49], off offset:256
	global_load_dwordx2 v[194:195], v[86:87], off offset:160
	global_load_dwordx4 v[222:225], v[48:49], off offset:320
	global_load_dwordx2 v[196:197], v[86:87], off offset:192
	global_load_dwordx4 v[226:229], v[48:49], off offset:384
	global_load_dwordx2 v[198:199], v[86:87], off offset:224
	global_load_dwordx4 v[230:233], v[48:49], off offset:448
	s_add_i32 s9, s18, 0
	s_mul_hi_i32 s21, s9, 36
	s_mul_i32 s9, s9, 36
	s_add_u32 s20, s9, s17
	s_addc_u32 s21, s21, s19
	s_lshl_b64 s[20:21], s[20:21], 16
	v_lshl_add_u64 v[86:87], v[102:103], 0, s[20:21]
	s_movk_i32 s76, 0x1000
	v_lshl_add_u64 v[92:93], v[86:87], 0, s[76:77]
	s_lshl_b32 s100, s66, 7
	s_mov_b32 m0, s100
	s_nop 0
	global_load_lds_dwordx4 v[86:87], off
	global_load_lds_dwordx4 v[86:87], off offset:1024
	global_load_lds_dwordx4 v[86:87], off offset:2048
	global_load_lds_dwordx4 v[86:87], off offset:3072
	s_add_i32 m0, s100, 0x1000
	s_nop 0
	global_load_lds_dwordx4 v[92:93], off
	global_load_lds_dwordx4 v[92:93], off offset:1024
	global_load_lds_dwordx4 v[92:93], off offset:2048
	global_load_lds_dwordx4 v[92:93], off offset:3072
	s_mov_b32 s76, 0x0
	v_lshl_add_u64 v[32:33], s[76:77], 0, v[52:53]
	v_lshlrev_b64 v[32:33], 10, v[32:33]
	v_lshl_add_u64 v[86:87], v[94:95], 0, v[32:33]
	global_load_dwordx4 v[104:107], v[86:87], off
	global_load_dwordx4 v[108:111], v[86:87], off offset:64
	global_load_dwordx4 v[112:115], v[86:87], off offset:128
	global_load_dwordx4 v[116:119], v[86:87], off offset:192
	s_add_i32 s9, s18, 16
	s_mul_hi_i32 s21, s9, 36
	s_mul_i32 s9, s9, 36
	s_add_u32 s20, s9, s17
	s_addc_u32 s21, s21, s19
	s_lshl_b64 s[20:21], s[20:21], 16
	v_lshl_add_u64 v[86:87], v[102:103], 0, s[20:21]
	s_movk_i32 s76, 0x1000
	v_lshl_add_u64 v[92:93], v[86:87], 0, s[76:77]
	s_lshl_b32 s100, s66, 7
	s_add_i32 s100, s100, 0x10000
	s_mov_b32 m0, s100
	s_nop 0
	global_load_lds_dwordx4 v[86:87], off
	global_load_lds_dwordx4 v[86:87], off offset:1024
	global_load_lds_dwordx4 v[86:87], off offset:2048
	global_load_lds_dwordx4 v[86:87], off offset:3072
	s_add_i32 m0, s100, 0x1000
	s_nop 0
	global_load_lds_dwordx4 v[92:93], off
	global_load_lds_dwordx4 v[92:93], off offset:1024
	global_load_lds_dwordx4 v[92:93], off offset:2048
	global_load_lds_dwordx4 v[92:93], off offset:3072
	s_mov_b32 s76, 0x2400
	v_lshl_add_u64 v[32:33], s[76:77], 0, v[52:53]
	v_lshlrev_b64 v[32:33], 10, v[32:33]
	v_lshl_add_u64 v[86:87], v[94:95], 0, v[32:33]
	global_load_dwordx4 v[250:253], v[86:87], off
	global_load_dwordx4 v[82:85], v[86:87], off offset:64
	global_load_dwordx4 v[98:101], v[86:87], off offset:128
	global_load_dwordx4 v[88:91], v[86:87], off offset:192
	s_mov_b32 s9, s77
	s_waitcnt vmcnt(40)
	v_lshlrev_b32_e32 v32, 16, v2
	v_and_b32_e32 v33, 0xffff0000, v2
	v_lshlrev_b32_e32 v34, 16, v3
	v_and_b32_e32 v35, 0xffff0000, v3
	v_lshlrev_b32_e32 v36, 16, v4
	v_and_b32_e32 v37, 0xffff0000, v4
	v_lshlrev_b32_e32 v38, 16, v5
	v_and_b32_e32 v39, 0xffff0000, v5
	v_lshlrev_b32_e32 v40, 16, v6
	v_and_b32_e32 v41, 0xffff0000, v6
	v_lshlrev_b32_e32 v42, 16, v7
	v_and_b32_e32 v43, 0xffff0000, v7
	v_lshlrev_b32_e32 v56, 16, v8
	v_and_b32_e32 v57, 0xffff0000, v8
	v_lshlrev_b32_e32 v58, 16, v9
	v_and_b32_e32 v59, 0xffff0000, v9
	v_lshlrev_b32_e32 v60, 16, v10
	v_and_b32_e32 v61, 0xffff0000, v10
	v_lshlrev_b32_e32 v66, 16, v11
	v_and_b32_e32 v67, 0xffff0000, v11
	v_lshlrev_b32_e32 v8, 16, v12
	v_and_b32_e32 v9, 0xffff0000, v12
	v_lshlrev_b32_e32 v10, 16, v13
	v_and_b32_e32 v11, 0xffff0000, v13
	v_lshlrev_b32_e32 v4, 16, v14
	v_and_b32_e32 v5, 0xffff0000, v14
	v_lshlrev_b32_e32 v6, 16, v15
	v_and_b32_e32 v7, 0xffff0000, v15
	v_lshlrev_b32_e32 v68, 16, v18
	v_and_b32_e32 v69, 0xffff0000, v18
	v_lshlrev_b32_e32 v70, 16, v19
	v_and_b32_e32 v71, 0xffff0000, v19
	v_lshlrev_b32_e32 v72, 16, v20
	v_and_b32_e32 v73, 0xffff0000, v20
	v_lshlrev_b32_e32 v20, 16, v21
	v_and_b32_e32 v21, 0xffff0000, v21
	v_lshlrev_b32_e32 v12, 16, v22
	v_and_b32_e32 v13, 0xffff0000, v22
	v_lshlrev_b32_e32 v14, 16, v23
	v_and_b32_e32 v15, 0xffff0000, v23
	v_lshlrev_b32_e32 v22, 16, v24
	v_and_b32_e32 v23, 0xffff0000, v24
	v_lshlrev_b32_e32 v18, 16, v25
	v_and_b32_e32 v19, 0xffff0000, v25
	v_lshlrev_b32_e32 v24, 16, v26
	v_and_b32_e32 v25, 0xffff0000, v26
	v_lshlrev_b32_e32 v26, 16, v27
	v_and_b32_e32 v27, 0xffff0000, v27
	v_lshlrev_b32_e32 v74, 16, v30
	v_and_b32_e32 v75, 0xffff0000, v30
	v_lshlrev_b32_e32 v30, 16, v31
	v_and_b32_e32 v31, 0xffff0000, v31
	v_lshlrev_b32_e32 v76, 16, v28
	v_and_b32_e32 v77, 0xffff0000, v28
	v_lshlrev_b32_e32 v28, 16, v29
	v_and_b32_e32 v29, 0xffff0000, v29
	v_lshlrev_b32_e32 v78, 16, v0
	v_and_b32_e32 v79, 0xffff0000, v0
	v_lshlrev_b32_e32 v80, 16, v16
	v_and_b32_e32 v81, 0xffff0000, v16
	v_lshlrev_b32_e32 v0, 16, v1
	v_lshlrev_b32_e32 v2, 16, v17
	v_and_b32_e32 v3, 0xffff0000, v17
	v_and_b32_e32 v1, 0xffff0000, v1
	v_pk_add_f32 v[2:3], v[0:1], v[2:3]
	v_pk_add_f32 v[0:1], v[78:79], v[80:81]
	v_pk_add_f32 v[6:7], v[6:7], v[30:31]
	v_pk_add_f32 v[4:5], v[4:5], v[74:75]
	v_pk_add_f32 v[10:11], v[10:11], v[26:27]
	v_pk_add_f32 v[8:9], v[8:9], v[24:25]
	v_pk_add_f32 v[18:19], v[66:67], v[18:19]
	v_pk_add_f32 v[16:17], v[60:61], v[22:23]
	v_pk_add_f32 v[14:15], v[58:59], v[14:15]
	v_pk_add_f32 v[12:13], v[56:57], v[12:13]
	v_pk_add_f32 v[22:23], v[42:43], v[20:21]
	v_pk_add_f32 v[20:21], v[40:41], v[72:73]
	v_pk_add_f32 v[26:27], v[38:39], v[70:71]
	v_pk_add_f32 v[24:25], v[36:37], v[68:69]
	v_pk_add_f32 v[30:31], v[34:35], v[28:29]
	v_pk_add_f32 v[28:29], v[32:33], v[76:77]
	s_waitcnt vmcnt(12)
	s_barrier
	ds_read_b128 v[120:123], v65
	ds_read_b128 v[124:127], v65 offset:4096
	ds_read_b128 v[128:131], v65 offset:8192
	ds_read_b128 v[132:135], v65 offset:12288
	ds_read_b128 v[136:139], v65 offset:16384
	ds_read_b128 v[140:143], v65 offset:20480
	ds_read_b128 v[144:147], v65 offset:24576
	ds_read_b128 v[148:151], v65 offset:28672
	ds_read_b128 v[152:155], v65 offset:1024
	ds_read_b128 v[156:159], v65 offset:5120
	ds_read_b128 v[160:163], v65 offset:9216
	ds_read_b128 v[164:167], v65 offset:13312
	ds_read_b128 v[168:171], v65 offset:17408
	ds_read_b128 v[172:175], v65 offset:21504
	ds_read_b128 v[176:179], v65 offset:25600
	ds_read_b128 v[180:183], v65 offset:29696
	s_waitcnt lgkmcnt(8)
	v_mfma_f32_16x16x32_bf16 v[28:31], v[120:123], v[104:107], v[28:31]
	v_mfma_f32_16x16x32_bf16 v[24:27], v[124:127], v[104:107], v[24:27]
	v_mfma_f32_16x16x32_bf16 v[20:23], v[128:131], v[104:107], v[20:23]
	v_mfma_f32_16x16x32_bf16 v[12:15], v[132:135], v[104:107], v[12:15]
	v_mfma_f32_16x16x32_bf16 v[16:19], v[136:139], v[104:107], v[16:19]
	v_mfma_f32_16x16x32_bf16 v[8:11], v[140:143], v[104:107], v[8:11]
	v_mfma_f32_16x16x32_bf16 v[4:7], v[144:147], v[104:107], v[4:7]
	v_mfma_f32_16x16x32_bf16 v[0:3], v[148:151], v[104:107], v[0:3]
	ds_read_b128 v[120:123], v65 offset:2048
	ds_read_b128 v[124:127], v65 offset:6144
	ds_read_b128 v[128:131], v65 offset:10240
	ds_read_b128 v[132:135], v65 offset:14336
	ds_read_b128 v[136:139], v65 offset:18432
	ds_read_b128 v[140:143], v65 offset:22528
	ds_read_b128 v[144:147], v65 offset:26624
	ds_read_b128 v[148:151], v65 offset:30720
	s_waitcnt lgkmcnt(8)
	v_mfma_f32_16x16x32_bf16 v[28:31], v[152:155], v[108:111], v[28:31]
	v_mfma_f32_16x16x32_bf16 v[24:27], v[156:159], v[108:111], v[24:27]
	v_mfma_f32_16x16x32_bf16 v[20:23], v[160:163], v[108:111], v[20:23]
	v_mfma_f32_16x16x32_bf16 v[12:15], v[164:167], v[108:111], v[12:15]
	v_mfma_f32_16x16x32_bf16 v[16:19], v[168:171], v[108:111], v[16:19]
	v_mfma_f32_16x16x32_bf16 v[8:11], v[172:175], v[108:111], v[8:11]
	v_mfma_f32_16x16x32_bf16 v[4:7], v[176:179], v[108:111], v[4:7]
	v_mfma_f32_16x16x32_bf16 v[0:3], v[180:183], v[108:111], v[0:3]
	ds_read_b128 v[152:155], v65 offset:3072
	ds_read_b128 v[156:159], v65 offset:7168
	ds_read_b128 v[160:163], v65 offset:11264
	ds_read_b128 v[164:167], v65 offset:15360
	ds_read_b128 v[168:171], v65 offset:19456
	ds_read_b128 v[172:175], v65 offset:23552
	ds_read_b128 v[176:179], v65 offset:27648
	ds_read_b128 v[180:183], v65 offset:31744
	s_waitcnt lgkmcnt(8)
	v_mfma_f32_16x16x32_bf16 v[28:31], v[120:123], v[112:115], v[28:31]
	v_mfma_f32_16x16x32_bf16 v[24:27], v[124:127], v[112:115], v[24:27]
	v_mfma_f32_16x16x32_bf16 v[20:23], v[128:131], v[112:115], v[20:23]
	v_mfma_f32_16x16x32_bf16 v[12:15], v[132:135], v[112:115], v[12:15]
	v_mfma_f32_16x16x32_bf16 v[16:19], v[136:139], v[112:115], v[16:19]
	v_mfma_f32_16x16x32_bf16 v[8:11], v[140:143], v[112:115], v[8:11]
	v_mfma_f32_16x16x32_bf16 v[4:7], v[144:147], v[112:115], v[4:7]
	v_mfma_f32_16x16x32_bf16 v[0:3], v[148:151], v[112:115], v[0:3]
	s_waitcnt lgkmcnt(0)
	v_mfma_f32_16x16x32_bf16 v[28:31], v[152:155], v[116:119], v[28:31]
	v_mfma_f32_16x16x32_bf16 v[24:27], v[156:159], v[116:119], v[24:27]
	v_mfma_f32_16x16x32_bf16 v[20:23], v[160:163], v[116:119], v[20:23]
	v_mfma_f32_16x16x32_bf16 v[12:15], v[164:167], v[116:119], v[12:15]
	v_mfma_f32_16x16x32_bf16 v[16:19], v[168:171], v[116:119], v[16:19]
	v_mfma_f32_16x16x32_bf16 v[8:11], v[172:175], v[116:119], v[8:11]
	v_mfma_f32_16x16x32_bf16 v[4:7], v[176:179], v[116:119], v[4:7]
	v_mfma_f32_16x16x32_bf16 v[0:3], v[180:183], v[116:119], v[0:3]
	s_waitcnt vmcnt(0)
	s_barrier
	v_add_u32_e32 v94, 0x10000, v65
	ds_read_b128 v[120:123], v94
	ds_read_b128 v[124:127], v94 offset:4096
	ds_read_b128 v[128:131], v94 offset:8192
	ds_read_b128 v[132:135], v94 offset:12288
	ds_read_b128 v[136:139], v94 offset:16384
	ds_read_b128 v[140:143], v94 offset:20480
	ds_read_b128 v[144:147], v94 offset:24576
	ds_read_b128 v[148:151], v94 offset:28672
	ds_read_b128 v[152:155], v94 offset:1024
	ds_read_b128 v[156:159], v94 offset:5120
	ds_read_b128 v[160:163], v94 offset:9216
	ds_read_b128 v[164:167], v94 offset:13312
	ds_read_b128 v[168:171], v94 offset:17408
	ds_read_b128 v[172:175], v94 offset:21504
	ds_read_b128 v[176:179], v94 offset:25600
	ds_read_b128 v[180:183], v94 offset:29696
	s_waitcnt lgkmcnt(8)
	v_mfma_f32_16x16x32_bf16 v[28:31], v[120:123], v[250:253], v[28:31]
	v_mfma_f32_16x16x32_bf16 v[24:27], v[124:127], v[250:253], v[24:27]
	v_mfma_f32_16x16x32_bf16 v[20:23], v[128:131], v[250:253], v[20:23]
	v_mfma_f32_16x16x32_bf16 v[12:15], v[132:135], v[250:253], v[12:15]
	v_mfma_f32_16x16x32_bf16 v[16:19], v[136:139], v[250:253], v[16:19]
	v_mfma_f32_16x16x32_bf16 v[8:11], v[140:143], v[250:253], v[8:11]
	v_mfma_f32_16x16x32_bf16 v[4:7], v[144:147], v[250:253], v[4:7]
	v_mfma_f32_16x16x32_bf16 v[0:3], v[148:151], v[250:253], v[0:3]
	ds_read_b128 v[120:123], v94 offset:2048
	ds_read_b128 v[124:127], v94 offset:6144
	ds_read_b128 v[128:131], v94 offset:10240
	ds_read_b128 v[132:135], v94 offset:14336
	ds_read_b128 v[136:139], v94 offset:18432
	ds_read_b128 v[140:143], v94 offset:22528
	ds_read_b128 v[144:147], v94 offset:26624
	ds_read_b128 v[148:151], v94 offset:30720
	s_waitcnt lgkmcnt(8)
	v_mfma_f32_16x16x32_bf16 v[28:31], v[152:155], v[82:85], v[28:31]
	v_mfma_f32_16x16x32_bf16 v[24:27], v[156:159], v[82:85], v[24:27]
	v_mfma_f32_16x16x32_bf16 v[20:23], v[160:163], v[82:85], v[20:23]
	v_mfma_f32_16x16x32_bf16 v[12:15], v[164:167], v[82:85], v[12:15]
	v_mfma_f32_16x16x32_bf16 v[16:19], v[168:171], v[82:85], v[16:19]
	v_mfma_f32_16x16x32_bf16 v[8:11], v[172:175], v[82:85], v[8:11]
	v_mfma_f32_16x16x32_bf16 v[4:7], v[176:179], v[82:85], v[4:7]
	v_mfma_f32_16x16x32_bf16 v[0:3], v[180:183], v[82:85], v[0:3]
	ds_read_b128 v[152:155], v94 offset:3072
	ds_read_b128 v[156:159], v94 offset:7168
	ds_read_b128 v[160:163], v94 offset:11264
	ds_read_b128 v[164:167], v94 offset:15360
	ds_read_b128 v[168:171], v94 offset:19456
	ds_read_b128 v[172:175], v94 offset:23552
	ds_read_b128 v[176:179], v94 offset:27648
	ds_read_b128 v[180:183], v94 offset:31744
	s_waitcnt lgkmcnt(8)
	v_mfma_f32_16x16x32_bf16 v[28:31], v[120:123], v[98:101], v[28:31]
	v_mfma_f32_16x16x32_bf16 v[24:27], v[124:127], v[98:101], v[24:27]
	v_mfma_f32_16x16x32_bf16 v[20:23], v[128:131], v[98:101], v[20:23]
	v_mfma_f32_16x16x32_bf16 v[12:15], v[132:135], v[98:101], v[12:15]
	v_mfma_f32_16x16x32_bf16 v[16:19], v[136:139], v[98:101], v[16:19]
	v_mfma_f32_16x16x32_bf16 v[8:11], v[140:143], v[98:101], v[8:11]
	v_mfma_f32_16x16x32_bf16 v[4:7], v[144:147], v[98:101], v[4:7]
	v_mfma_f32_16x16x32_bf16 v[0:3], v[148:151], v[98:101], v[0:3]
	s_waitcnt lgkmcnt(0)
	v_mfma_f32_16x16x32_bf16 v[28:31], v[152:155], v[88:91], v[28:31]
	v_mfma_f32_16x16x32_bf16 v[24:27], v[156:159], v[88:91], v[24:27]
	v_mfma_f32_16x16x32_bf16 v[20:23], v[160:163], v[88:91], v[20:23]
	v_mfma_f32_16x16x32_bf16 v[12:15], v[164:167], v[88:91], v[12:15]
	v_mfma_f32_16x16x32_bf16 v[16:19], v[168:171], v[88:91], v[16:19]
	v_mfma_f32_16x16x32_bf16 v[8:11], v[172:175], v[88:91], v[8:11]
	v_mfma_f32_16x16x32_bf16 v[4:7], v[176:179], v[88:91], v[4:7]
	v_mfma_f32_16x16x32_bf16 v[0:3], v[180:183], v[88:91], v[0:3]
	s_nop 1
	v_mul_f32_e32 v32, v29, v29
	v_mul_f32_e32 v33, v25, v25
	v_fmac_f32_e32 v32, v28, v28
	v_fmac_f32_e32 v33, v24, v24
	v_fmac_f32_e32 v32, v30, v30
	v_fmac_f32_e32 v33, v26, v26
	v_fmac_f32_e32 v32, v31, v31
	v_fmac_f32_e32 v33, v27, v27
	v_add_f32_e32 v32, v32, v33
	v_mul_f32_e32 v33, v21, v21
	v_fmac_f32_e32 v33, v20, v20
	v_fmac_f32_e32 v33, v22, v22
	v_fmac_f32_e32 v33, v23, v23
	v_add_f32_e32 v32, v32, v33
	v_mul_f32_e32 v33, v13, v13
	v_fmac_f32_e32 v33, v12, v12
	v_fmac_f32_e32 v33, v14, v14
	v_fmac_f32_e32 v33, v15, v15
	v_add_f32_e32 v32, v32, v33
	v_mul_f32_e32 v33, v17, v17
	v_fmac_f32_e32 v33, v16, v16
	v_fmac_f32_e32 v33, v18, v18
	v_fmac_f32_e32 v33, v19, v19
	v_add_f32_e32 v32, v32, v33
	v_mul_f32_e32 v33, v9, v9
	v_fmac_f32_e32 v33, v8, v8
	v_fmac_f32_e32 v33, v10, v10
	v_fmac_f32_e32 v33, v11, v11
	v_add_f32_e32 v32, v32, v33
	v_mul_f32_e32 v33, v5, v5
	v_fmac_f32_e32 v33, v4, v4
	v_fmac_f32_e32 v33, v6, v6
	v_fmac_f32_e32 v33, v7, v7
	v_add_f32_e32 v32, v32, v33
	v_mul_f32_e32 v33, v1, v1
	v_fmac_f32_e32 v33, v0, v0
	v_fmac_f32_e32 v33, v2, v2
	v_fmac_f32_e32 v33, v3, v3
	v_add_f32_e32 v32, v32, v33
	ds_swizzle_b32 v33, v32 offset:swizzle(SWAP,16)
	s_waitcnt lgkmcnt(0)
	s_barrier
	v_add_f32_e32 v32, v32, v33
	v_mov_b32_e32 v33, v32
	s_nop 1
	v_permlane32_swap_b32_e32 v32, v33
	s_and_saveexec_b64 s[10:11], s[2:3]
	s_cbranch_execz .LBB0_1053
	v_add_f32_e32 v32, v32, v33
	ds_write_b32 v64, v32
	s_branch .LBB0_1053
